# conversion source loads: workgroup-scope non-temporal (sc0 nt) instead of nt
# baseline (speedup 1.0000x reference)
; __device__ __forceinline__ void finishSM(f32x16& p0, f32x16& p1, float alpha, float& l_reg, bf16x8& pa0, bf16x8& pa1, bf16x8& pa2, bf16x8& pa3) {
; #pragma unroll
;   for (int r = 0; r < 16; ++r) p1[r] = __builtin_amdgcn_exp2f(p1[r]);
;   float ps = 0;
; #pragma unroll
;   for (int r = 0; r < 16; ++r) ps += p0[r];
; #pragma unroll
;   for (int r = 0; r < 16; ++r) ps += p1[r];
;   { auto rr = __builtin_amdgcn_permlane32_swap(__float_as_uint(ps), __float_as_uint(ps), false, false);
;     ps = __uint_as_float(rr[0]) + __uint_as_float(rr[1]); }
;   l_reg = l_reg * alpha + ps;
;     ...
;   PK4(p0, 0, pa0); PK4(p0, 8, pa1); PK4(p1, 0, pa2); PK4(p1, 8, pa3);
;     ...
; }
; __device__ __forceinline__ void qkt(f32x16& p0, f32x16& p1, const bf16_t* Ks, const bf16x8* qr, int r32, int hi) {
;   p0 = f32x16{}; p1 = f32x16{};
; #pragma unroll
;   for (int d0 = 0; d0 < 8; ++d0) { int cb = (d0 * 16 + hi * 8) * 2;
;     bf16x8 b0 = *reinterpret_cast<const bf16x8*>((const char*)Ks + KSWZ(r32, cb));
;     bf16x8 b1 = *reinterpret_cast<const bf16x8*>((const char*)Ks + KSWZ(32 + r32, cb));
;     p0 = __builtin_amdgcn_mfma_f32_32x32x16_bf16(b0, qr[d0], p0, 0, 0, 0);
;     p1 = __builtin_amdgcn_mfma_f32_32x32x16_bf16(b1, qr[d0], p1, 0, 0, 0); }
.LBB0_510:
	ds_read_b128 v[64:67], v200 offset:49152
	ds_read_b128 v[68:71], v200 offset:57344
	ds_read_b128 v[212:215], v202 offset:49152
	ds_read_b128 v[216:219], v202 offset:57344
	v_add_f32_e32 v160, 0, v175
	v_add_f32_e32 v160, v210, v160
	s_waitcnt lgkmcnt(3)
	v_mfma_f32_32x32x16_bf16 v[80:95], v[64:67], v[116:119], 0
	v_add_f32_e32 v160, v161, v160
	v_add_f32_e32 v160, v207, v160
	v_add_f32_e32 v160, v162, v160
	v_add_f32_e32 v160, v174, v160
	v_add_f32_e32 v160, v163, v160
	v_add_f32_e32 v160, v173, v160
	v_add_f32_e32 v160, v164, v160
	s_waitcnt lgkmcnt(2)
	v_mfma_f32_32x32x16_bf16 v[64:79], v[68:71], v[116:119], 0
	v_add_f32_e32 v160, v172, v160
	v_add_f32_e32 v160, v165, v160
	v_add_f32_e32 v160, v171, v160
	v_exp_f32_e32 v156, v156
	v_add_f32_e32 v160, v166, v160
	v_exp_f32_e32 v157, v157
	v_add_f32_e32 v160, v170, v160
	s_waitcnt lgkmcnt(1)
	v_mfma_f32_32x32x16_bf16 v[80:95], v[212:215], v[112:115], v[80:95]
	v_exp_f32_e32 v154, v154
	v_add_f32_e32 v160, v167, v160
	v_exp_f32_e32 v155, v155
	v_add_f32_e32 v160, v169, v160
	v_exp_f32_e32 v148, v148
	v_add_f32_e32 v160, v156, v160
	v_exp_f32_e32 v149, v149
	s_waitcnt lgkmcnt(0)
	v_mfma_f32_32x32x16_bf16 v[64:79], v[216:219], v[112:115], v[64:79]
	ds_read_b128 v[212:215], v201 offset:49152
	ds_read_b128 v[216:219], v201 offset:57344
	v_add_f32_e32 v160, v157, v160
	v_exp_f32_e32 v146, v146
	v_add_f32_e32 v160, v154, v160
	v_exp_f32_e32 v147, v147
	v_add_f32_e32 v160, v155, v160
	v_exp_f32_e32 v144, v144
	s_waitcnt lgkmcnt(1)
	v_mfma_f32_32x32x16_bf16 v[80:95], v[212:215], v[124:127], v[80:95]
	v_add_f32_e32 v160, v148, v160
	v_exp_f32_e32 v145, v145
	v_add_f32_e32 v160, v149, v160
	v_exp_f32_e32 v158, v158
	v_add_f32_e32 v160, v146, v160
	v_exp_f32_e32 v159, v159
	v_add_f32_e32 v160, v147, v160
	s_waitcnt lgkmcnt(0)
	v_mfma_f32_32x32x16_bf16 v[64:79], v[216:219], v[124:127], v[64:79]
	ds_read_b128 v[212:215], v198 offset:49152
	ds_read_b128 v[216:219], v198 offset:57344
	v_exp_f32_e32 v152, v152
	v_add_f32_e32 v160, v144, v160
	v_exp_f32_e32 v153, v153
	v_add_f32_e32 v160, v145, v160
	v_exp_f32_e32 v150, v150
	v_add_f32_e32 v160, v158, v160
	s_waitcnt lgkmcnt(1)
	v_mfma_f32_32x32x16_bf16 v[80:95], v[212:215], v[120:123], v[80:95]
	v_exp_f32_e32 v151, v151
	v_add_f32_e32 v160, v159, v160
	v_add_f32_e32 v160, v152, v160
	v_add_f32_e32 v160, v153, v160
	v_add_f32_e32 v160, v150, v160
	v_add_f32_e32 v204, v151, v160
	v_mov_b32_e32 v205, v204
	s_waitcnt lgkmcnt(0)
	v_mfma_f32_32x32x16_bf16 v[64:79], v[216:219], v[120:123], v[64:79]
	ds_read_b128 v[212:215], v197 offset:49152
	ds_read_b128 v[216:219], v197 offset:57344
	v_permlane32_swap_b32_e32 v204, v205
	s_waitcnt lgkmcnt(1)
	v_mfma_f32_32x32x16_bf16 v[80:95], v[212:215], v[108:111], v[80:95]
	s_waitcnt lgkmcnt(0)
	v_mfma_f32_32x32x16_bf16 v[64:79], v[216:219], v[108:111], v[64:79]
	ds_read_b128 v[212:215], v196 offset:49152
	ds_read_b128 v[216:219], v196 offset:57344
	s_waitcnt lgkmcnt(1)
	v_mfma_f32_32x32x16_bf16 v[80:95], v[212:215], v[104:107], v[80:95]
	s_waitcnt lgkmcnt(0)
	v_mfma_f32_32x32x16_bf16 v[64:79], v[216:219], v[104:107], v[64:79]
	ds_read_b128 v[212:215], v195 offset:49152
	ds_read_b128 v[216:219], v195 offset:57344
	s_waitcnt lgkmcnt(1)
	v_mfma_f32_32x32x16_bf16 v[80:95], v[212:215], v[100:103], v[80:95]
	s_waitcnt lgkmcnt(0)
	v_mfma_f32_32x32x16_bf16 v[64:79], v[216:219], v[100:103], v[64:79]
	ds_read_b128 v[212:215], v192 offset:49152
	ds_read_b128 v[216:219], v192 offset:57344
	v_cvt_pk_bf16_f32 v160, v175, v210
	v_cvt_pk_bf16_f32 v161, v161, v207
	v_cvt_pk_bf16_f32 v162, v162, v174
	v_cvt_pk_bf16_f32 v163, v163, v173
	v_cvt_pk_bf16_f32 v164, v164, v172
	v_cvt_pk_bf16_f32 v165, v165, v171
	s_waitcnt lgkmcnt(1)
	v_mfma_f32_32x32x16_bf16 v[80:95], v[212:215], v[96:99], v[80:95]
	v_cvt_pk_bf16_f32 v166, v166, v170
	v_cvt_pk_bf16_f32 v167, v167, v169
	v_cvt_pk_bf16_f32 v170, v156, v157
	v_cvt_pk_bf16_f32 v171, v154, v155
	v_cvt_pk_bf16_f32 v172, v148, v149
	v_cvt_pk_bf16_f32 v173, v146, v147
	v_cvt_pk_bf16_f32 v206, v144, v145
	s_waitcnt lgkmcnt(0)
	v_mfma_f32_32x32x16_bf16 v[64:79], v[216:219], v[96:99], v[64:79]
	v_cvt_pk_bf16_f32 v207, v158, v159
	v_cvt_pk_bf16_f32 v208, v152, v153
	v_permlane32_swap_b32_e32 v160, v162
	v_cvt_pk_bf16_f32 v209, v150, v151
	v_permlane32_swap_b32_e32 v206, v208
	v_permlane32_swap_b32_e32 v161, v163
	v_permlane32_swap_b32_e32 v164, v166
	v_permlane32_swap_b32_e32 v165, v167
	v_permlane32_swap_b32_e32 v170, v172
	v_permlane32_swap_b32_e32 v171, v173
	v_permlane32_swap_b32_e32 v207, v209
	s_mov_b32 s4, 0xff6e8000
	v_add_co_u32_e32 v144, vcc, s4, v178
	s_mov_b32 s4, 0xff6f0000
	s_nop 0
	v_addc_co_u32_e32 v145, vcc, -1, v179, vcc
	v_add_co_u32_e32 v148, vcc, s4, v178
	s_mov_b32 s4, 0xfffe8000
	s_nop 0
	v_addc_co_u32_e32 v149, vcc, -1, v179, vcc
	v_add_co_u32_e32 v152, vcc, s4, v178
	s_mov_b32 s4, 0xffff0000
	s_nop 0
	v_addc_co_u32_e32 v153, vcc, -1, v179, vcc
	v_add_co_u32_e32 v156, vcc, s4, v178
	global_load_dwordx4 v[144:147], v[144:145], off
	s_nop 0
	global_load_dwordx4 v[148:151], v[148:149], off
	v_addc_co_u32_e32 v157, vcc, -1, v179, vcc
	global_load_dwordx4 v[152:155], v[152:153], off
	s_nop 0
	global_load_dwordx4 v[156:159], v[156:157], off
	s_min_u32 s101, s99, 31
	v_mov_b32_e32 v253, s101
	v_and_b32_e32 v253, 3, v253
	s_lshr_b32 s100, s101, 2
	s_add_i32 s100, s100, 32
	s_lshl_b32 s100, s100, 11
	s_and_b32 s101, s98, 0x7ff
	s_add_i32 s100, s100, s101
	s_sub_i32 s101, s100, 0x10000
	s_lshr_b32 s101, s101, 10
	s_lshl_b32 s101, s101, 24
	v_mov_b32_e32 v252, s101
	s_bfe_u32 s101, s100, 0x40006
	s_lshl_b32 s101, s101, 20
	v_add_u32_e32 v252, s101, v252
	s_and_b32 s101, s100, 63
	s_lshl_b32 s101, s101, 7
	v_add_u32_e32 v252, s101, v252
	v_mbcnt_lo_u32_b32 v251, -1, 0
	v_mbcnt_hi_u32_b32 v251, -1, v251
	v_lshrrev_b32_e32 v250, 3, v251
	v_and_b32_e32 v251, 7, v251
	v_lshl_add_u32 v252, v250, 17, v252
	v_lshl_add_u32 v252, v251, 4, v252
	v_lshl_add_u32 v252, v253, 15, v252
	v_readlane_b32 s100, v254, 42
	v_readlane_b32 s101, v254, 43
	s_nop 4
	global_load_dwordx4 v[232:235], v252, s[100:101] sc0 nt
	v_add_u32_e32 v252, 0x2000, v252
	global_load_dwordx4 v[236:239], v252, s[100:101] sc0 nt
	v_add_u32_e32 v252, 0x2000, v252
	global_load_dwordx4 v[240:243], v252, s[100:101] sc0 nt
	v_add_u32_e32 v252, 0x2000, v252
	global_load_dwordx4 v[244:247], v252, s[100:101] sc0 nt
	ds_read_b64_tr_b16 v[210:211], v190 offset:0
	ds_read_b64_tr_b16 v[212:213], v190 offset:0x800
	ds_read_b64_tr_b16 v[214:215], v190 offset:0x1000
	ds_read_b64_tr_b16 v[216:217], v190 offset:0x1800
	ds_read_b64_tr_b16 v[218:219], v190 offset:0x2000
	ds_read_b64_tr_b16 v[220:221], v190 offset:0x2800
	ds_read_b64_tr_b16 v[222:223], v190 offset:0x3000
	ds_read_b64_tr_b16 v[224:225], v190 offset:0x3800
	s_waitcnt lgkmcnt(0)
; #define SWRITE(b, i) do { *(bf16x8*)((char*)V_lds + (b) * SHM_V + vst0) = sr_[i].vs0;          \
;     *(bf16x8*)((char*)V_lds + (b) * SHM_V + vst1) = sr_[i].vs1; int kc = sc * 2;               \
;     *(bf16x8*)((char*)K_lds + (b) * SHM_K + KSWZ(sr, kc)) = sr_[i].ks0;                       \
;     *(bf16x8*)((char*)K_lds + (b) * SHM_K + KSWZ(32 + sr, kc)) = sr_[i].ks1; } while (0)
; #define SWAIT() do { asm volatile("s_waitcnt vmcnt(4)" ::: "memory"); } while (0)
; #define RESC(a) do { if (__any((a) < 1.f)) { if (hi == 0) al_l[r32] = (a); asm volatile("s_waitcnt lgkmcnt(0)" ::: "memory"); \
;     _Pragma("unroll") for (int d = 0; d < 4; ++d) _Pragma("unroll") for (int r = 0; r < 16; ++r) o[d][r] *= al_l[crow(r, hi)]; } } while (0)
; __device__ __forceinline__ void partialSM(f32x16& p0, f32x16& p1, float& m_reg, float& mn, float& alpha) {
;   constexpr float C = SCALE * 1.4426950408889634f;
;   float pmax = p0[0];
; #pragma unroll
;   for (int r = 1; r < 16; ++r) pmax = fmaxf(pmax, p0[r]);
; #pragma unroll
;   for (int r = 0; r < 16; ++r) pmax = fmaxf(pmax, p1[r]);
;   { auto rr = __builtin_amdgcn_permlane32_swap(__float_as_uint(pmax), __float_as_uint(pmax), false, false);
;     pmax = fmaxf(__uint_as_float(rr[0]), __uint_as_float(rr[1])); }
;   if (__builtin_expect(__all(pmax - m_reg <= THR / SCALE), 1)) { mn = m_reg; alpha = 1.f; }
;   else { mn = fmaxf(m_reg, pmax); alpha = __builtin_amdgcn_exp2f((m_reg - mn) * C); m_reg = mn; }
; __device__ __forceinline__ void attn_dense_body(const bf16_t* __restrict__ Qb, const bf16_t* __restrict__ Kh, const bf16_t* __restrict__ Vh,
;                                                 unsigned char* __restrict__ Ob, int seq, char* lds, LAS unsigned char* lds3, const int wave_) {
;     ...
;     pv_d0(o, vb0, pa0, pa1, pa2, pa3); partialSM(pB0, pB1, m_reg, mnB, alB);
;     __syncthreads(); SWAIT(); SWRITE(0, SE);
;     RESC(alB); __syncthreads();
	s_nop 0
	v_mfma_f32_32x32x16_bf16 v[0:15], v[160:163], v[210:213], v[0:15]
	ds_read_b64_tr_b16 v[210:211], v190 offset:0x200
	ds_read_b64_tr_b16 v[212:213], v190 offset:0xa00
	v_mfma_f32_32x32x16_bf16 v[0:15], v[164:167], v[214:217], v[0:15]
	ds_read_b64_tr_b16 v[214:215], v190 offset:0x1200
	ds_read_b64_tr_b16 v[216:217], v190 offset:0x1a00
	v_mfma_f32_32x32x16_bf16 v[0:15], v[170:173], v[218:221], v[0:15]
	ds_read_b64_tr_b16 v[218:219], v190 offset:0x2200
	ds_read_b64_tr_b16 v[220:221], v190 offset:0x2a00
	v_mfma_f32_32x32x16_bf16 v[0:15], v[206:209], v[222:225], v[0:15]
	ds_read_b64_tr_b16 v[222:223], v190 offset:0x3200
	ds_read_b64_tr_b16 v[224:225], v190 offset:0x3a00
	s_waitcnt lgkmcnt(0)
	v_mfma_f32_32x32x16_bf16 v[48:63], v[160:163], v[210:213], v[48:63]
	ds_read_b64_tr_b16 v[210:211], v190 offset:0x400
	ds_read_b64_tr_b16 v[212:213], v190 offset:0xc00
	v_mfma_f32_32x32x16_bf16 v[48:63], v[164:167], v[214:217], v[48:63]
	ds_read_b64_tr_b16 v[214:215], v190 offset:0x1400
	ds_read_b64_tr_b16 v[216:217], v190 offset:0x1c00
	v_mfma_f32_32x32x16_bf16 v[48:63], v[170:173], v[218:221], v[48:63]
	ds_read_b64_tr_b16 v[218:219], v190 offset:0x2400
	ds_read_b64_tr_b16 v[220:221], v190 offset:0x2c00
	v_mfma_f32_32x32x16_bf16 v[48:63], v[206:209], v[222:225], v[48:63]
	ds_read_b64_tr_b16 v[222:223], v190 offset:0x3400
	ds_read_b64_tr_b16 v[224:225], v190 offset:0x3c00
	s_waitcnt lgkmcnt(0)
	v_mfma_f32_32x32x16_bf16 v[32:47], v[160:163], v[210:213], v[32:47]
	ds_read_b64_tr_b16 v[210:211], v190 offset:0x600
	ds_read_b64_tr_b16 v[212:213], v190 offset:0xe00
	v_mfma_f32_32x32x16_bf16 v[32:47], v[164:167], v[214:217], v[32:47]
	ds_read_b64_tr_b16 v[214:215], v190 offset:0x1600
	ds_read_b64_tr_b16 v[216:217], v190 offset:0x1e00
	v_mfma_f32_32x32x16_bf16 v[32:47], v[170:173], v[218:221], v[32:47]
	ds_read_b64_tr_b16 v[218:219], v190 offset:0x2600
	ds_read_b64_tr_b16 v[220:221], v190 offset:0x2e00
	v_mfma_f32_32x32x16_bf16 v[32:47], v[206:209], v[222:225], v[32:47]
	ds_read_b64_tr_b16 v[222:223], v190 offset:0x3600
	ds_read_b64_tr_b16 v[224:225], v190 offset:0x3e00
	s_waitcnt lgkmcnt(0)
	v_mfma_f32_32x32x16_bf16 v[16:31], v[160:163], v[210:213], v[16:31]
	v_max_f32_e32 v160, v81, v81
	v_max_f32_e32 v161, v80, v80
	v_max_f32_e32 v160, v161, v160
	v_max3_f32 v160, v160, v82, v83
	v_max3_f32 v160, v160, v84, v85
	v_max3_f32 v160, v160, v86, v87
	v_max3_f32 v160, v160, v88, v89
	v_max3_f32 v160, v160, v90, v91
	v_max3_f32 v160, v160, v92, v93
	v_mfma_f32_32x32x16_bf16 v[16:31], v[164:167], v[214:217], v[16:31]
	v_max3_f32 v160, v160, v94, v95
	v_max3_f32 v160, v160, v64, v65
	v_max3_f32 v160, v160, v66, v67
	v_max3_f32 v160, v160, v68, v69
	v_max3_f32 v160, v160, v70, v71
	v_max3_f32 v160, v160, v72, v73
	v_max3_f32 v160, v160, v74, v75
	v_max3_f32 v160, v160, v76, v77
	v_mfma_f32_32x32x16_bf16 v[16:31], v[170:173], v[218:221], v[16:31]
	v_max3_f32 v160, v160, v78, v79
	v_mov_b32_e32 v161, v160
	s_nop 1
	v_permlane32_swap_b32_e32 v160, v161
	v_max_f32_e32 v161, v161, v161
	v_max_f32_e32 v160, v160, v160
	v_max_f32_e32 v160, v160, v161
	v_sub_f32_e32 v161, v160, v168
	v_cmp_ge_f32_e32 vcc, s52, v161
	v_max_f32_e32 v161, v168, v168
	v_max_f32_e32 v160, v161, v160
	v_mfma_f32_32x32x16_bf16 v[16:31], v[206:209], v[222:225], v[16:31]
	v_sub_f32_e32 v161, v168, v160
	v_mul_f32_e32 v161, 0x3e0293ee, v161
	v_exp_f32_e32 v161, v161
	s_cmp_eq_u64 vcc, exec
	s_cselect_b64 s[4:5], -1, 0
	s_barrier
	s_waitcnt vmcnt(8)
	v_cndmask_b32_e64 v206, v161, 1.0, s[4:5]
	v_cmp_gt_f32_e32 vcc, 1.0, v206
	s_waitcnt vmcnt(8)
	ds_write_b128 v193, v[128:131]
	ds_write_b128 v194, v[132:135]
	ds_write_b128 v191, v[136:139] offset:32768
	ds_write_b128 v199, v[140:143] offset:32768
	s_cbranch_vccz .LBB0_514
	s_and_saveexec_b64 s[34:35], s[2:3]
	ds_write_b32 v187, v206 offset:128
	s_or_b64 exec, exec, s[34:35]
	s_waitcnt lgkmcnt(0)
	v_add_u32_e32 v161, s29, v176
	ds_read_b128 v[162:165], v161 offset:224
	ds_read_b128 v[170:173], v161 offset:192
	ds_read_b128 v[208:211], v161 offset:160
	ds_read_b128 v[212:215], v161 offset:128
	s_waitcnt lgkmcnt(3)
	v_pk_mul_f32 v[12:13], v[12:13], v[162:163]
	s_waitcnt lgkmcnt(2)
	v_pk_mul_f32 v[8:9], v[8:9], v[170:171]
	s_waitcnt lgkmcnt(1)
	v_pk_mul_f32 v[4:5], v[4:5], v[208:209]
	v_pk_mul_f32 v[14:15], v[14:15], v[164:165]
	v_pk_mul_f32 v[10:11], v[10:11], v[172:173]
	v_pk_mul_f32 v[6:7], v[6:7], v[210:211]
	s_waitcnt lgkmcnt(0)
	v_pk_mul_f32 v[2:3], v[2:3], v[214:215]
	v_pk_mul_f32 v[0:1], v[0:1], v[212:213]
	v_pk_mul_f32 v[60:61], v[60:61], v[162:163]
	v_pk_mul_f32 v[56:57], v[56:57], v[170:171]
	v_pk_mul_f32 v[52:53], v[52:53], v[208:209]
	v_pk_mul_f32 v[62:63], v[62:63], v[164:165]
	v_pk_mul_f32 v[58:59], v[58:59], v[172:173]
	v_pk_mul_f32 v[54:55], v[54:55], v[210:211]
	v_pk_mul_f32 v[50:51], v[50:51], v[214:215]
	v_pk_mul_f32 v[48:49], v[48:49], v[212:213]
	v_pk_mul_f32 v[44:45], v[44:45], v[162:163]
	v_pk_mul_f32 v[40:41], v[40:41], v[170:171]
	v_pk_mul_f32 v[36:37], v[36:37], v[208:209]
	v_pk_mul_f32 v[46:47], v[46:47], v[164:165]
	v_pk_mul_f32 v[42:43], v[42:43], v[172:173]
	v_pk_mul_f32 v[38:39], v[38:39], v[210:211]
	v_pk_mul_f32 v[34:35], v[34:35], v[214:215]
	v_pk_mul_f32 v[32:33], v[32:33], v[212:213]
	v_pk_mul_f32 v[28:29], v[28:29], v[162:163]
	v_pk_mul_f32 v[24:25], v[24:25], v[170:171]
	v_pk_mul_f32 v[20:21], v[20:21], v[208:209]
	v_pk_mul_f32 v[30:31], v[30:31], v[164:165]
	v_pk_mul_f32 v[26:27], v[26:27], v[172:173]
	v_pk_mul_f32 v[22:23], v[22:23], v[210:211]
	v_pk_mul_f32 v[18:19], v[18:19], v[214:215]
	v_pk_mul_f32 v[16:17], v[16:17], v[212:213]

.LBB0_573:
	s_and_b32 s37, s37, 0x780
	v_add_u32_e32 v68, s37, v146
	v_ashrrev_i32_e32 v69, 31, v68
	v_lshlrev_b64 v[68:69], s64, v[68:69]
	s_lshl_b32 s37, s38, 2
	s_lshl_b32 s38, s33, 7
	v_lshl_add_u64 v[68:69], s[72:73], 0, v[68:69]
	s_and_b32 s38, s38, s37
	s_mov_b32 s39, s79
	v_lshl_add_u64 v[68:69], v[68:69], 0, s[38:39]
	v_lshlrev_b32_e32 v70, 2, v148
	v_mov_b32_e32 v71, v141
	v_lshl_add_u64 v[124:125], v[68:69], 0, v[70:71]
	v_lshl_add_u64 v[72:73], v[124:125], 0, s[60:61]
	v_lshl_add_u64 v[76:77], v[124:125], 0, s[58:59]
	v_lshl_add_u64 v[80:81], v[124:125], 0, s[2:3]
	v_lshl_add_u64 v[84:85], v[124:125], 0, s[70:71]
	v_lshl_add_u64 v[88:89], v[124:125], 0, s[68:69]
	v_lshl_add_u64 v[92:93], v[124:125], 0, s[34:35]
	v_lshl_add_u64 v[96:97], v[124:125], 0, s[54:55]
	v_lshl_add_u64 v[100:101], v[124:125], 0, s[66:67]
	v_lshl_add_u64 v[104:105], v[124:125], 0, s[52:53]
	v_lshl_add_u64 v[108:109], v[124:125], 0, s[84:85]
	v_lshl_add_u64 v[112:113], v[124:125], 0, s[74:75]
	v_lshl_add_u64 v[116:117], v[124:125], 0, s[86:87]
	v_lshl_add_u64 v[120:121], v[124:125], 0, vcc
	v_lshl_add_u64 v[126:127], v[124:125], 0, s[96:97]
	v_lshl_add_u64 v[128:129], v[124:125], 0, s[30:31]
	global_load_dwordx4 v[68:71], v[124:125], off sc0 nt
	s_nop 0
	global_load_dwordx4 v[72:75], v[72:73], off sc0 nt
	s_nop 0
	global_load_dwordx4 v[76:79], v[76:77], off sc0 nt
	s_nop 0
	global_load_dwordx4 v[80:83], v[80:81], off sc0 nt
	s_nop 0
	global_load_dwordx4 v[84:87], v[84:85], off sc0 nt
	s_nop 0
	global_load_dwordx4 v[88:91], v[88:89], off sc0 nt
	s_nop 0
	global_load_dwordx4 v[92:95], v[92:93], off sc0 nt
	s_nop 0
	global_load_dwordx4 v[96:99], v[96:97], off sc0 nt
	s_nop 0
	global_load_dwordx4 v[100:103], v[100:101], off sc0 nt
	s_nop 0
	global_load_dwordx4 v[104:107], v[104:105], off sc0 nt
	s_nop 0
	global_load_dwordx4 v[108:111], v[108:109], off sc0 nt
	s_nop 0
	global_load_dwordx4 v[112:115], v[112:113], off sc0 nt
	s_nop 0
	global_load_dwordx4 v[116:119], v[116:117], off sc0 nt
	s_nop 0
	global_load_dwordx4 v[120:123], v[120:121], off sc0 nt
	s_nop 0
	global_load_dwordx4 v[124:127], v[126:127], off sc0 nt
	s_nop 0
	global_load_dwordx4 v[128:131], v[128:129], off sc0 nt
	v_readlane_b32 s74, v255, 25

; __device__ __forceinline__ void mlstm_unit(LAS unsigned char* lds, const bf16_t* __restrict__ PM, const float* __restrict__ GATES, bf16_t* __restrict__ Hout,
;                                            int b, int h, int dir, int vs, Conv& cvs, const int wave_) {
;     ...
;         CV_FINISH();
;         if ((ci % 3) == 0) { CV_ISSUE(); pend_b = true; }
.LBB0_614:
	s_and_b32 s0, s0, 0x780
	s_waitcnt vmcnt(15)
	v_add_u32_e32 v68, s0, v146
	v_ashrrev_i32_e32 v69, 31, v68
	v_lshlrev_b64 v[68:69], s64, v[68:69]
	s_lshl_b32 s0, s36, 2
	s_lshl_b32 s36, s33, 7
	v_lshl_add_u64 v[68:69], s[72:73], 0, v[68:69]
	s_and_b32 s36, s36, s0
	s_mov_b32 s37, s79
	v_lshl_add_u64 v[68:69], v[68:69], 0, s[36:37]
	v_lshlrev_b32_e32 v70, 2, v148
	v_mov_b32_e32 v71, v141
	s_waitcnt vmcnt(1)
	v_lshl_add_u64 v[124:125], v[68:69], 0, v[70:71]
	v_lshl_add_u64 v[72:73], v[124:125], 0, s[60:61]
	v_lshl_add_u64 v[76:77], v[124:125], 0, s[58:59]
	v_lshl_add_u64 v[80:81], v[124:125], 0, s[2:3]
	v_lshl_add_u64 v[84:85], v[124:125], 0, s[70:71]
	v_lshl_add_u64 v[88:89], v[124:125], 0, s[68:69]
	v_lshl_add_u64 v[92:93], v[124:125], 0, s[34:35]
	v_lshl_add_u64 v[96:97], v[124:125], 0, s[54:55]
	v_lshl_add_u64 v[100:101], v[124:125], 0, s[66:67]
	v_lshl_add_u64 v[104:105], v[124:125], 0, s[52:53]
	v_lshl_add_u64 v[108:109], v[124:125], 0, s[84:85]
	v_lshl_add_u64 v[112:113], v[124:125], 0, s[74:75]
	v_lshl_add_u64 v[116:117], v[124:125], 0, s[86:87]
	v_lshl_add_u64 v[120:121], v[124:125], 0, s[96:97]
	v_lshl_add_u64 v[126:127], v[124:125], 0, s[94:95]
	s_waitcnt vmcnt(0)
	v_lshl_add_u64 v[128:129], v[124:125], 0, s[92:93]
	global_load_dwordx4 v[68:71], v[124:125], off sc0 nt
	s_nop 0
	global_load_dwordx4 v[72:75], v[72:73], off sc0 nt
	s_nop 0
	global_load_dwordx4 v[76:79], v[76:77], off sc0 nt
	s_nop 0
	global_load_dwordx4 v[80:83], v[80:81], off sc0 nt
	s_nop 0
	global_load_dwordx4 v[84:87], v[84:85], off sc0 nt
	s_nop 0
	global_load_dwordx4 v[88:91], v[88:89], off sc0 nt
	s_nop 0
	global_load_dwordx4 v[92:95], v[92:93], off sc0 nt
	s_nop 0
	global_load_dwordx4 v[96:99], v[96:97], off sc0 nt
	s_nop 0
	global_load_dwordx4 v[100:103], v[100:101], off sc0 nt
	s_nop 0
	global_load_dwordx4 v[104:107], v[104:105], off sc0 nt
	s_nop 0
	global_load_dwordx4 v[108:111], v[108:109], off sc0 nt
	s_nop 0
	global_load_dwordx4 v[112:115], v[112:113], off sc0 nt
	s_nop 0
	global_load_dwordx4 v[116:119], v[116:117], off sc0 nt
	s_nop 0
	global_load_dwordx4 v[120:123], v[120:121], off sc0 nt
	s_nop 0
	global_load_dwordx4 v[124:127], v[126:127], off sc0 nt
	s_nop 0
	global_load_dwordx4 v[128:131], v[128:129], off sc0 nt
	v_readlane_b32 s74, v255, 25

; __global__ void __launch_bounds__(NTHREADS, 2) fwd(Args args) {
;     ...
;             {
;                 f32x4 cv[16];
; #pragma unroll 1
;                 while (cvs.t < ml::T_CONV) { CV_ISSUE(); CV_FINISH(); }
.LBB0_632:
	s_and_b32 s2, s2, 0x780
	v_add_u32_e32 v0, s2, v64
	v_ashrrev_i32_e32 v1, 31, v0
	v_lshlrev_b64 v[0:1], s58, v[0:1]
	s_and_b32 s2, s0, s40
	v_lshl_add_u64 v[0:1], s[6:7], 0, v[0:1]
	s_lshl_b32 s2, s2, 2
	v_lshl_add_u64 v[0:1], v[0:1], 0, s[2:3]
	v_lshl_add_u64 v[60:61], v[0:1], 0, v[70:71]
	v_lshl_add_u64 v[56:57], v[60:61], 0, s[54:55]
	v_lshl_add_u64 v[52:53], v[60:61], 0, s[52:53]
	v_lshl_add_u64 v[48:49], v[60:61], 0, s[34:35]
	v_lshl_add_u64 v[44:45], v[60:61], 0, s[30:31]
	v_lshl_add_u64 v[40:41], v[60:61], 0, s[28:29]
	v_lshl_add_u64 v[36:37], v[60:61], 0, s[26:27]
	v_lshl_add_u64 v[32:33], v[60:61], 0, s[24:25]
	v_lshl_add_u64 v[28:29], v[60:61], 0, s[22:23]
	v_lshl_add_u64 v[24:25], v[60:61], 0, s[20:21]
	v_lshl_add_u64 v[20:21], v[60:61], 0, s[18:19]
	v_lshl_add_u64 v[16:17], v[60:61], 0, s[16:17]
	v_lshl_add_u64 v[12:13], v[60:61], 0, s[14:15]
	v_lshl_add_u64 v[8:9], v[60:61], 0, s[12:13]
	v_lshl_add_u64 v[4:5], v[60:61], 0, s[10:11]
	v_lshl_add_u64 v[0:1], v[60:61], 0, s[8:9]
	global_load_dwordx4 v[0:3], v[0:1], off sc0 nt
	s_nop 0
	global_load_dwordx4 v[4:7], v[4:5], off sc0 nt
	s_nop 0
	global_load_dwordx4 v[8:11], v[8:9], off sc0 nt
	s_nop 0
	global_load_dwordx4 v[12:15], v[12:13], off sc0 nt
	s_nop 0
	global_load_dwordx4 v[16:19], v[16:17], off sc0 nt
	s_nop 0
	global_load_dwordx4 v[20:23], v[20:21], off sc0 nt
	s_nop 0
	global_load_dwordx4 v[24:27], v[24:25], off sc0 nt
	s_nop 0
	global_load_dwordx4 v[28:31], v[28:29], off sc0 nt
	s_nop 0
	global_load_dwordx4 v[32:35], v[32:33], off sc0 nt
	s_nop 0
	global_load_dwordx4 v[36:39], v[36:37], off sc0 nt
	s_nop 0
	global_load_dwordx4 v[40:43], v[40:41], off sc0 nt
	s_nop 0
	global_load_dwordx4 v[44:47], v[44:45], off sc0 nt
	s_nop 0
	global_load_dwordx4 v[48:51], v[48:49], off sc0 nt
	s_nop 0
	global_load_dwordx4 v[52:55], v[52:53], off sc0 nt
	s_nop 0
	global_load_dwordx4 v[56:59], v[56:57], off sc0 nt
	s_nop 0
	global_load_dwordx4 v[60:63], v[60:61], off sc0 nt
	s_mov_b64 s[6:7], -1
	s_and_b64 vcc, exec, s[4:5]
	s_cbranch_vccz .LBB0_634
	s_add_i32 s2, s33, 0xffff0000
	s_lshr_b32 s2, s2, 10
	s_and_b32 s4, s36, 0x3f0000
	v_or_b32_e32 v68, s4, v67
	s_lshl_b64 s[4:5], s[2:3], 22
	v_readlane_b32 s2, v255, 18
	s_add_u32 s4, s2, s4
	v_readlane_b32 s2, v255, 19
	s_addc_u32 s5, s2, s5
	v_lshl_add_u64 v[72:73], s[4:5], 0, v[68:69]
	s_lshl_b32 s2, s33, 1
	s_mov_b64 s[6:7], 0

; template <class Epi, class Sched, class Ops, bool FP8 = false>
; __device__ __forceinline__ void gemm_phase(LAS unsigned char* lds, const int RB, const Sched& S, const Ops& G, const Epi& E, const int wave_) {
;     ...
;         if constexpr (FP8) {
;             asm volatile("s_nop 15\n\ts_nop 15" ::: "memory");
; #pragma unroll
;             for (int a = 0; a < 2; ++a)
; #pragma unroll
;                 for (int b = 0; b < 2; ++b)
; #pragma unroll
;                     for (int m = 0; m < 4; ++m) asm volatile("" : "+v"(acc[a][b][m][0]), "+v"(acc[a][b][m][1]));
;         }
;         E(acc, cur, wr, wc, fr, fq);
;     __device__ __forceinline__ void operator()(const g8::Acc& acc, const g8::Unit& u, int wr, int wc, int fr, int fq) const {
;         const int row0 = u.pm * 256 + wr * 64 + fr, j0 = u.pn * 128 + wc * 32 + 8 * fq;
;         const float* bg = bgu + (size_t)u.e * 4096 + j0; const float* bu = bg + 2048;
;         const f32x4 g0 = *(const f32x4*)bg, g1 = *(const f32x4*)(bg + 4), u0 = *(const f32x4*)bu, u1 = *(const f32x4*)(bu + 4);
.LBB0_1178:
	s_nop 15
	s_nop 15
	s_and_b64 vcc, exec, s[8:9]
	s_cbranch_vccz .LBB0_1139
	v_ashrrev_i32_e32 v197, 31, v196
	v_readlane_b32 s80, v254, 34
	v_lshl_add_u32 v220, s58, 7, v231
	v_lshlrev_b64 v[66:67], 14, v[196:197]
	v_readlane_b32 s86, v254, 40
	v_readlane_b32 s87, v254, 41
	v_ashrrev_i32_e32 v221, 31, v220
	v_lshl_add_u32 v222, s78, 8, v230
	v_lshl_add_u64 v[66:67], s[86:87], 0, v[66:67]
	v_lshl_add_u64 v[66:67], v[220:221], 2, v[66:67]
	global_load_dwordx4 v[208:211], v[66:67], off
	global_load_dwordx4 v[200:203], v[66:67], off offset:16
	v_add_co_u32_e32 v196, vcc, 0x2000, v66
	v_readlane_b32 s81, v254, 35
	s_nop 0
	v_addc_co_u32_e32 v197, vcc, 0, v67, vcc
	v_lshl_add_u64 v[66:67], v[66:67], 0, s[52:53]
	global_load_dwordx4 v[204:207], v[196:197], off
	s_and_b64 vcc, exec, s[4:5]
	global_load_dwordx4 v[196:199], v[66:67], off offset:16
	v_readlane_b32 s82, v254, 36
	v_readlane_b32 s83, v254, 37
	v_readlane_b32 s84, v254, 38
	v_readlane_b32 s85, v254, 39
	v_readlane_b32 s88, v254, 42
	v_readlane_b32 s89, v254, 43
	v_readlane_b32 s90, v254, 44
	v_readlane_b32 s91, v254, 45
	v_readlane_b32 s92, v254, 46
	v_readlane_b32 s93, v254, 47
	v_readlane_b32 s94, v254, 48
	v_readlane_b32 s95, v254, 49
	s_mov_b32 s99, 0
	s_cmp_lt_u32 s98, 0x18000
	s_cbranch_scc0 .Lp9e_noissue
	s_mov_b32 s99, s98
	v_mbcnt_lo_u32_b32 v244, -1, 0
	v_mbcnt_hi_u32_b32 v244, -1, v244
	s_sub_i32 s100, s99, 0x10000
	s_lshr_b32 s100, s100, 10
	s_lshl_b32 s100, s100, 24
	s_bfe_u32 s101, s99, 0x40006
	s_lshl_b32 s101, s101, 20
	s_add_i32 s100, s100, s101
	s_and_b32 s101, s99, 63
	s_lshl_b32 s101, s101, 7
	s_add_i32 s100, s100, s101
	v_lshrrev_b32_e32 v245, 3, v244
	v_and_b32_e32 v246, 7, v244
	v_lshlrev_b32_e32 v245, 17, v245
	v_lshl_or_b32 v245, v246, 4, v245
	v_add_u32_e32 v245, s100, v245
	v_readlane_b32 s100, v254, 42
	v_readlane_b32 s101, v254, 43
	s_nop 4
	global_load_dwordx4 v[0:3], v245, s[100:101] sc0 nt
	v_add_u32_e32 v245, 0x2000, v245
	global_load_dwordx4 v[4:7], v245, s[100:101] sc0 nt
	v_add_u32_e32 v245, 0x2000, v245
	global_load_dwordx4 v[8:11], v245, s[100:101] sc0 nt
	v_add_u32_e32 v245, 0x2000, v245
	global_load_dwordx4 v[12:15], v245, s[100:101] sc0 nt
	v_add_u32_e32 v245, 0x2000, v245
	global_load_dwordx4 v[16:19], v245, s[100:101] sc0 nt
	v_add_u32_e32 v245, 0x2000, v245
	global_load_dwordx4 v[20:23], v245, s[100:101] sc0 nt
	v_add_u32_e32 v245, 0x2000, v245
	global_load_dwordx4 v[24:27], v245, s[100:101] sc0 nt
	v_add_u32_e32 v245, 0x2000, v245
	global_load_dwordx4 v[28:31], v245, s[100:101] sc0 nt
	v_add_u32_e32 v245, 0x2000, v245
	global_load_dwordx4 v[32:35], v245, s[100:101] sc0 nt
	v_add_u32_e32 v245, 0x2000, v245
	global_load_dwordx4 v[36:39], v245, s[100:101] sc0 nt
	v_add_u32_e32 v245, 0x2000, v245
	global_load_dwordx4 v[40:43], v245, s[100:101] sc0 nt
	v_add_u32_e32 v245, 0x2000, v245
	global_load_dwordx4 v[44:47], v245, s[100:101] sc0 nt
	v_add_u32_e32 v245, 0x2000, v245
	global_load_dwordx4 v[48:51], v245, s[100:101] sc0 nt
	v_add_u32_e32 v245, 0x2000, v245
	global_load_dwordx4 v[52:55], v245, s[100:101] sc0 nt
	v_add_u32_e32 v245, 0x2000, v245
	global_load_dwordx4 v[56:59], v245, s[100:101] sc0 nt
	v_add_u32_e32 v245, 0x2000, v245
	global_load_dwordx4 v[60:63], v245, s[100:101] sc0 nt
	s_waitcnt vmcnt(16)
	s_branch .Lp9e_joined

; __global__ void __launch_bounds__(NTHREADS, 2) fwd(Args args) {
;     ...
;                 f32x4 cv[16];
; #pragma unroll 1
;                 while (cvs.t < ml::T_CONV) { CV_ISSUE(); CV_FINISH(); }
.LBB0_1184:
.Lp9_cl_loop:
	s_cmp_lt_u32 s98, 0x18000
	s_cbranch_scc0 .Lp9_cl_done
	s_mov_b32 s99, s98
	v_mbcnt_lo_u32_b32 v244, -1, 0
	v_mbcnt_hi_u32_b32 v244, -1, v244
	s_sub_i32 s100, s99, 0x10000
	s_lshr_b32 s100, s100, 10
	s_lshl_b32 s100, s100, 24
	s_bfe_u32 s101, s99, 0x40006
	s_lshl_b32 s101, s101, 20
	s_add_i32 s100, s100, s101
	s_and_b32 s101, s99, 63
	s_lshl_b32 s101, s101, 7
	s_add_i32 s100, s100, s101
	v_lshrrev_b32_e32 v245, 3, v244
	v_and_b32_e32 v246, 7, v244
	v_lshlrev_b32_e32 v245, 17, v245
	v_lshl_or_b32 v245, v246, 4, v245
	v_add_u32_e32 v245, s100, v245
	v_readlane_b32 s100, v254, 42
	v_readlane_b32 s101, v254, 43
	s_nop 4
	global_load_dwordx4 v[0:3], v245, s[100:101] sc0 nt
	v_add_u32_e32 v245, 0x2000, v245
	global_load_dwordx4 v[4:7], v245, s[100:101] sc0 nt
	v_add_u32_e32 v245, 0x2000, v245
	global_load_dwordx4 v[8:11], v245, s[100:101] sc0 nt
	v_add_u32_e32 v245, 0x2000, v245
	global_load_dwordx4 v[12:15], v245, s[100:101] sc0 nt
	v_add_u32_e32 v245, 0x2000, v245
	global_load_dwordx4 v[16:19], v245, s[100:101] sc0 nt
	v_add_u32_e32 v245, 0x2000, v245
	global_load_dwordx4 v[20:23], v245, s[100:101] sc0 nt
	v_add_u32_e32 v245, 0x2000, v245
	global_load_dwordx4 v[24:27], v245, s[100:101] sc0 nt
	v_add_u32_e32 v245, 0x2000, v245
	global_load_dwordx4 v[28:31], v245, s[100:101] sc0 nt
	v_add_u32_e32 v245, 0x2000, v245
	global_load_dwordx4 v[32:35], v245, s[100:101] sc0 nt
	v_add_u32_e32 v245, 0x2000, v245
	global_load_dwordx4 v[36:39], v245, s[100:101] sc0 nt
	v_add_u32_e32 v245, 0x2000, v245
	global_load_dwordx4 v[40:43], v245, s[100:101] sc0 nt
	v_add_u32_e32 v245, 0x2000, v245
	global_load_dwordx4 v[44:47], v245, s[100:101] sc0 nt
	v_add_u32_e32 v245, 0x2000, v245
	global_load_dwordx4 v[48:51], v245, s[100:101] sc0 nt
	v_add_u32_e32 v245, 0x2000, v245
	global_load_dwordx4 v[52:55], v245, s[100:101] sc0 nt
	v_add_u32_e32 v245, 0x2000, v245
	global_load_dwordx4 v[56:59], v245, s[100:101] sc0 nt
	v_add_u32_e32 v245, 0x2000, v245
	global_load_dwordx4 v[60:63], v245, s[100:101] sc0 nt
	s_sub_i32 s100, s99, 0x10000
	s_lshr_b32 s100, s100, 10
	s_lshl_b32 s100, s100, 22
	s_and_b32 s101, s99, 63
	s_lshl_b32 s101, s101, 16
	s_add_i32 s100, s100, s101
	s_bfe_u32 s101, s99, 0x40006
	s_lshl_b32 s101, s101, 7
	s_add_i32 s100, s100, s101
	v_mbcnt_lo_u32_b32 v244, -1, 0
	v_mbcnt_hi_u32_b32 v244, -1, v244
	v_lshrrev_b32_e32 v245, 3, v244
	v_and_b32_e32 v246, 7, v244
	v_lshlrev_b32_e32 v245, 4, v245
	v_lshl_or_b32 v245, v246, 13, v245
	v_add_u32_e32 v245, s100, v245
	v_readlane_b32 s100, v254, 48
	v_readlane_b32 s101, v254, 49
	s_add_u32 s100, s100, 0x14d59400
	s_addc_u32 s101, s101, 0
	s_waitcnt vmcnt(0)
	v_mul_f32_e32 v246, 0x42000000, v0
	v_mul_f32_e32 v247, 0x42000000, v4
	v_mov_b32_e32 v248, 0
	v_cvt_pk_fp8_f32 v248, v246, v247
	v_mul_f32_e32 v246, 0x42000000, v8
	v_mul_f32_e32 v247, 0x42000000, v12
	v_cvt_pk_fp8_f32 v248, v246, v247 op_sel:[0,0,1]
	v_mul_f32_e32 v246, 0x42000000, v16
	v_mul_f32_e32 v247, 0x42000000, v20
	v_mov_b32_e32 v249, 0
	v_cvt_pk_fp8_f32 v249, v246, v247
	v_mul_f32_e32 v246, 0x42000000, v24
	v_mul_f32_e32 v247, 0x42000000, v28
	v_cvt_pk_fp8_f32 v249, v246, v247 op_sel:[0,0,1]
	v_mul_f32_e32 v246, 0x42000000, v32
	v_mul_f32_e32 v247, 0x42000000, v36
	v_mov_b32_e32 v250, 0
	v_cvt_pk_fp8_f32 v250, v246, v247
	v_mul_f32_e32 v246, 0x42000000, v40
	v_mul_f32_e32 v247, 0x42000000, v44
	v_cvt_pk_fp8_f32 v250, v246, v247 op_sel:[0,0,1]
	v_mul_f32_e32 v246, 0x42000000, v48
	v_mul_f32_e32 v247, 0x42000000, v52
	v_mov_b32_e32 v251, 0
	v_cvt_pk_fp8_f32 v251, v246, v247
	v_mul_f32_e32 v246, 0x42000000, v56
	v_mul_f32_e32 v247, 0x42000000, v60
	v_cvt_pk_fp8_f32 v251, v246, v247 op_sel:[0,0,1]
	s_nop 0
	global_store_dwordx4 v245, v[248:251], s[100:101] nt
	v_mul_f32_e32 v246, 0x42000000, v1
	v_mul_f32_e32 v247, 0x42000000, v5
	v_mov_b32_e32 v248, 0
	v_cvt_pk_fp8_f32 v248, v246, v247
	v_mul_f32_e32 v246, 0x42000000, v9
	v_mul_f32_e32 v247, 0x42000000, v13
	v_cvt_pk_fp8_f32 v248, v246, v247 op_sel:[0,0,1]
	v_mul_f32_e32 v246, 0x42000000, v17
	v_mul_f32_e32 v247, 0x42000000, v21
	v_mov_b32_e32 v249, 0
	v_cvt_pk_fp8_f32 v249, v246, v247
	v_mul_f32_e32 v246, 0x42000000, v25
	v_mul_f32_e32 v247, 0x42000000, v29
	v_cvt_pk_fp8_f32 v249, v246, v247 op_sel:[0,0,1]
	v_mul_f32_e32 v246, 0x42000000, v33
	v_mul_f32_e32 v247, 0x42000000, v37
	v_mov_b32_e32 v250, 0
	v_cvt_pk_fp8_f32 v250, v246, v247
	v_mul_f32_e32 v246, 0x42000000, v41
	v_mul_f32_e32 v247, 0x42000000, v45
	v_cvt_pk_fp8_f32 v250, v246, v247 op_sel:[0,0,1]
	v_mul_f32_e32 v246, 0x42000000, v49
	v_mul_f32_e32 v247, 0x42000000, v53
	v_mov_b32_e32 v251, 0
	v_cvt_pk_fp8_f32 v251, v246, v247
	v_mul_f32_e32 v246, 0x42000000, v57
	v_mul_f32_e32 v247, 0x42000000, v61
	v_cvt_pk_fp8_f32 v251, v246, v247 op_sel:[0,0,1]
	s_nop 0
	global_store_dwordx4 v245, v[248:251], s[100:101] offset:2048 nt
	v_add_u32_e32 v245, 0x1000, v245
	v_mul_f32_e32 v246, 0x42000000, v2
	v_mul_f32_e32 v247, 0x42000000, v6
	v_mov_b32_e32 v248, 0
	v_cvt_pk_fp8_f32 v248, v246, v247
	v_mul_f32_e32 v246, 0x42000000, v10
	v_mul_f32_e32 v247, 0x42000000, v14
	v_cvt_pk_fp8_f32 v248, v246, v247 op_sel:[0,0,1]
	v_mul_f32_e32 v246, 0x42000000, v18
	v_mul_f32_e32 v247, 0x42000000, v22
	v_mov_b32_e32 v249, 0
	v_cvt_pk_fp8_f32 v249, v246, v247
	v_mul_f32_e32 v246, 0x42000000, v26
	v_mul_f32_e32 v247, 0x42000000, v30
	v_cvt_pk_fp8_f32 v249, v246, v247 op_sel:[0,0,1]
	v_mul_f32_e32 v246, 0x42000000, v34
	v_mul_f32_e32 v247, 0x42000000, v38
	v_mov_b32_e32 v250, 0
	v_cvt_pk_fp8_f32 v250, v246, v247
	v_mul_f32_e32 v246, 0x42000000, v42
	v_mul_f32_e32 v247, 0x42000000, v46
	v_cvt_pk_fp8_f32 v250, v246, v247 op_sel:[0,0,1]
	v_mul_f32_e32 v246, 0x42000000, v50
	v_mul_f32_e32 v247, 0x42000000, v54
	v_mov_b32_e32 v251, 0
	v_cvt_pk_fp8_f32 v251, v246, v247
	v_mul_f32_e32 v246, 0x42000000, v58
	v_mul_f32_e32 v247, 0x42000000, v62
	v_cvt_pk_fp8_f32 v251, v246, v247 op_sel:[0,0,1]
	s_nop 0
	global_store_dwordx4 v245, v[248:251], s[100:101] nt
	v_mul_f32_e32 v246, 0x42000000, v3
	v_mul_f32_e32 v247, 0x42000000, v7
	v_mov_b32_e32 v248, 0
	v_cvt_pk_fp8_f32 v248, v246, v247
	v_mul_f32_e32 v246, 0x42000000, v11
	v_mul_f32_e32 v247, 0x42000000, v15
	v_cvt_pk_fp8_f32 v248, v246, v247 op_sel:[0,0,1]
	v_mul_f32_e32 v246, 0x42000000, v19
	v_mul_f32_e32 v247, 0x42000000, v23
	v_mov_b32_e32 v249, 0
	v_cvt_pk_fp8_f32 v249, v246, v247
	v_mul_f32_e32 v246, 0x42000000, v27
	v_mul_f32_e32 v247, 0x42000000, v31
	v_cvt_pk_fp8_f32 v249, v246, v247 op_sel:[0,0,1]
	v_mul_f32_e32 v246, 0x42000000, v35
	v_mul_f32_e32 v247, 0x42000000, v39
	v_mov_b32_e32 v250, 0
	v_cvt_pk_fp8_f32 v250, v246, v247
	v_mul_f32_e32 v246, 0x42000000, v43
	v_mul_f32_e32 v247, 0x42000000, v47
	v_cvt_pk_fp8_f32 v250, v246, v247 op_sel:[0,0,1]
	v_mul_f32_e32 v246, 0x42000000, v51
	v_mul_f32_e32 v247, 0x42000000, v55
	v_mov_b32_e32 v251, 0
	v_cvt_pk_fp8_f32 v251, v246, v247
	v_mul_f32_e32 v246, 0x42000000, v59
	v_mul_f32_e32 v247, 0x42000000, v63
	v_cvt_pk_fp8_f32 v251, v246, v247 op_sel:[0,0,1]
	s_nop 0
	global_store_dwordx4 v245, v[248:251], s[100:101] offset:2048 nt
	s_add_i32 s98, s98, 0x800
	s_mov_b32 s99, 0
	s_branch .Lp9_cl_loop
